# baseline (speedup 1.0000x reference)
.LBB3_2:
	v_readfirstlane_b32 s24, v0
	s_lshr_b32 s35, s24, 6
	s_lshl_b32 s36, s26, 8
	s_lshl_b32 s12, s26, 3
	s_add_u32 s12, s14, s12
	s_addc_u32 s23, s15, 0
	s_add_u32 s22, s12, s35
	s_addc_u32 s23, s23, 0
	s_lshl_b64 s[22:23], s[22:23], 12
	s_lshl_b32 s12, s35, 10
	s_cmp_lg_u32 0, -1
	v_lshl_add_u64 v[18:19], v[208:209], 0, s[22:23]
	s_cselect_b32 s22, 0, 0
	v_lshl_add_u64 v[198:199], v[210:211], 0, s[12:13]
	s_add_i32 s39, s12, s22
	s_mov_b32 s22, m0
	s_mov_b32 m0, s39
	s_nop 0
	global_load_lds_dwordx4 v[198:199], off
	s_mov_b32 m0, s22
	v_lshl_add_u64 v[98:99], v[212:213], 0, s[12:13]
	s_add_i32 s40, s39, 0x6000
	s_mov_b32 s22, m0
	s_mov_b32 m0, s40
	s_nop 0
	global_load_lds_dwordx4 v[98:99], off
	s_mov_b32 m0, s22
	v_lshl_add_u64 v[20:21], v[198:199], 0, s[4:5]
	s_add_i32 s22, s39, 0x2000
	s_mov_b32 s23, m0
	s_mov_b32 m0, s22
	s_nop 0
	global_load_lds_dwordx4 v[20:21], off
	s_mov_b32 m0, s23
	global_load_dwordx4 v[154:157], v[18:19], off
	global_load_dwordx4 v[146:149], v[18:19], off offset:1024
	global_load_dwordx4 v[138:141], v[18:19], off offset:2048
	global_load_dwordx4 v[130:133], v[18:19], off offset:3072
	v_mov_b64_e32 v[32:33], v[16:17]
	v_mov_b64_e32 v[30:31], v[14:15]
	v_mov_b64_e32 v[28:29], v[12:13]
	v_mov_b64_e32 v[26:27], v[10:11]
	v_mov_b64_e32 v[24:25], v[8:9]
	v_mov_b64_e32 v[22:23], v[6:7]
	v_mov_b64_e32 v[20:21], v[4:5]
	v_mov_b64_e32 v[18:19], v[2:3]
	v_lshl_add_u64 v[34:35], v[198:199], 0, s[6:7]
	s_add_i32 s22, s39, 0x4000
	s_mov_b32 s23, m0
	s_mov_b32 m0, s22
	s_nop 0
	global_load_lds_dwordx4 v[34:35], off
	s_mov_b32 m0, s23
	s_waitcnt vmcnt(3) lgkmcnt(0)
	s_barrier
	ds_read_b128 v[50:53], v226
	ds_read_b128 v[54:57], v226 offset:512
	s_lshl_b32 s37, s35, 5
	s_cmp_lg_u32 s26, 0
	s_cselect_b64 s[22:23], -1, 0
	v_or_b32_e32 v219, s37, v1
	s_and_b64 vcc, exec, s[22:23]
	s_waitcnt vmcnt(3) lgkmcnt(1)
	v_mfma_f32_32x32x16_f16 v[34:49], v[50:53], v[154:157], v[18:33]
	s_waitcnt lgkmcnt(0)
	v_mfma_f32_32x32x16_f16 v[18:33], v[54:57], v[154:157], v[18:33]
	ds_read_b128 v[50:53], v226 offset:2048
	ds_read_b128 v[54:57], v226 offset:2560
	s_waitcnt vmcnt(2) lgkmcnt(1)
	v_mfma_f32_32x32x16_f16 v[34:49], v[50:53], v[146:149], v[34:49]
	s_waitcnt lgkmcnt(0)
	v_mfma_f32_32x32x16_f16 v[18:33], v[54:57], v[146:149], v[18:33]
	ds_read_b128 v[50:53], v226 offset:4096
	ds_read_b128 v[54:57], v226 offset:4608
	s_waitcnt vmcnt(1) lgkmcnt(1)
	v_mfma_f32_32x32x16_f16 v[34:49], v[50:53], v[138:141], v[34:49]
	s_waitcnt lgkmcnt(0)
	v_mfma_f32_32x32x16_f16 v[18:33], v[54:57], v[138:141], v[18:33]
	ds_read_b128 v[50:53], v226 offset:6144
	ds_read_b128 v[54:57], v226 offset:6656
	s_waitcnt vmcnt(0) lgkmcnt(1)
	v_mfma_f32_32x32x16_f16 v[34:49], v[50:53], v[130:133], v[34:49]
	s_waitcnt lgkmcnt(0)
	v_mfma_f32_32x32x16_f16 v[18:33], v[54:57], v[130:133], v[18:33]
	s_nop 15
	s_nop 7
	s_cbranch_vccnz .LBB3_4
	s_cmp_ge_u32 s35, 2
	s_cbranch_scc1 .LBB3_4
	v_sub_u32_e32 v50, v219, v228
	s_cmp_eq_u32 s35, 1
	s_cbranch_scc1 .Lmd1_p
	v_cmp_lt_i32_e32 vcc, 0, v50
	s_nop 1
	v_cndmask_b32_e32 v35, v241, v35, vcc
	v_cmp_le_i32_e32 vcc, 0, v50
	s_nop 1
	v_cndmask_b32_e32 v34, v241, v34, vcc
	v_cmp_le_i32_e32 vcc, 2, v50
	s_nop 1
	v_cndmask_b32_e32 v36, v241, v36, vcc
	v_cmp_le_i32_e32 vcc, 3, v50
	s_nop 1
	v_cndmask_b32_e32 v37, v241, v37, vcc
	v_cmp_le_i32_e32 vcc, 8, v50
	s_nop 1
	v_cndmask_b32_e32 v38, v241, v38, vcc
	v_cmp_le_i32_e32 vcc, 9, v50
	s_nop 1
	v_cndmask_b32_e32 v39, v241, v39, vcc
	v_cmp_le_i32_e32 vcc, 10, v50
	s_nop 1
	v_cndmask_b32_e32 v40, v241, v40, vcc
	v_cmp_le_i32_e32 vcc, 11, v50
	s_nop 1
	v_cndmask_b32_e32 v41, v241, v41, vcc
	v_cmp_le_i32_e32 vcc, 16, v50
	s_nop 1
	v_cndmask_b32_e32 v42, v241, v42, vcc
	v_cmp_le_i32_e32 vcc, 17, v50
	s_nop 1
	v_cndmask_b32_e32 v43, v241, v43, vcc
	v_cmp_le_i32_e32 vcc, 18, v50
	s_nop 1
	v_cndmask_b32_e32 v44, v241, v44, vcc
	v_cmp_le_i32_e32 vcc, 19, v50
	s_nop 1
	v_cndmask_b32_e32 v45, v241, v45, vcc
	v_cmp_le_i32_e32 vcc, 24, v50
	s_nop 1
	v_cndmask_b32_e32 v46, v241, v46, vcc
	v_cmp_le_i32_e32 vcc, 25, v50
	s_nop 1
	v_cndmask_b32_e32 v47, v241, v47, vcc
	v_cmp_le_i32_e32 vcc, 26, v50
	s_nop 1
	v_cndmask_b32_e32 v48, v241, v48, vcc
	v_cmp_le_i32_e32 vcc, 27, v50
	s_nop 1
	v_cndmask_b32_e32 v49, v241, v49, vcc
	v_mov_b32_e32 v18, v241
	v_mov_b32_e32 v19, v241
	v_mov_b32_e32 v20, v241
	v_mov_b32_e32 v21, v241
	v_mov_b32_e32 v22, v241
	v_mov_b32_e32 v23, v241
	v_mov_b32_e32 v24, v241
	v_mov_b32_e32 v25, v241
	v_mov_b32_e32 v26, v241
	v_mov_b32_e32 v27, v241
	v_mov_b32_e32 v28, v241
	v_mov_b32_e32 v29, v241
	v_mov_b32_e32 v30, v241
	v_mov_b32_e32 v31, v241
	v_mov_b32_e32 v32, v241
	v_mov_b32_e32 v33, v241
	s_branch .LBB3_4
.Lmd1_p:
	v_cmp_le_i32_e32 vcc, 32, v50
	s_nop 1
	v_cndmask_b32_e32 v18, v241, v18, vcc
	v_cmp_le_i32_e32 vcc, 33, v50
	s_nop 1
	v_cndmask_b32_e32 v19, v241, v19, vcc
	v_cmp_le_i32_e32 vcc, 34, v50
	s_nop 1
	v_cndmask_b32_e32 v20, v241, v20, vcc
	v_cmp_le_i32_e32 vcc, 35, v50
	s_nop 1
	v_cndmask_b32_e32 v21, v241, v21, vcc
	v_cmp_le_i32_e32 vcc, 40, v50
	s_nop 1
	v_cndmask_b32_e32 v22, v241, v22, vcc
	v_cmp_le_i32_e32 vcc, 41, v50
	s_nop 1
	v_cndmask_b32_e32 v23, v241, v23, vcc
	v_cmp_le_i32_e32 vcc, 42, v50
	s_nop 1
	v_cndmask_b32_e32 v24, v241, v24, vcc
	v_cmp_le_i32_e32 vcc, 43, v50
	s_nop 1
	v_cndmask_b32_e32 v25, v241, v25, vcc
	v_cmp_le_i32_e32 vcc, 48, v50
	s_nop 1
	v_cndmask_b32_e32 v26, v241, v26, vcc
	v_cmp_le_i32_e32 vcc, 49, v50
	s_nop 1
	v_cndmask_b32_e32 v27, v241, v27, vcc
	v_cmp_le_i32_e32 vcc, 50, v50
	s_nop 1
	v_cndmask_b32_e32 v28, v241, v28, vcc
	v_cmp_le_i32_e32 vcc, 51, v50
	s_nop 1
	v_cndmask_b32_e32 v29, v241, v29, vcc
	v_cmp_le_i32_e32 vcc, 56, v50
	s_nop 1
	v_cndmask_b32_e32 v30, v241, v30, vcc
	v_cmp_le_i32_e32 vcc, 57, v50
	s_nop 1
	v_cndmask_b32_e32 v31, v241, v31, vcc
	v_cmp_le_i32_e32 vcc, 58, v50
	s_nop 1
	v_cndmask_b32_e32 v32, v241, v32, vcc
	v_cmp_le_i32_e32 vcc, 59, v50
	s_nop 1
	v_cndmask_b32_e32 v33, v241, v33, vcc
